# speedup vs baseline: 1.0031x; 1.0031x over previous
_Z9proj_gemmPKfS0_S0_PK14__hip_bfloat16S0_S0_S0_PS1_:
	s_bitcmp1_b32 s2, 3
	s_cbranch_scc0 .Lno_sleep
	s_sleep 40
